# baseline (speedup 1.0000x reference)
.Lkf_par_done:
	s_mov_b64 exec, -1
	v_lshlrev_b32_e32 v4, 4, v4
	v_lshlrev_b32_e32 v5, 6, v5
	v_lshl_or_b32 v3, v3, 2, v4
	v_lshlrev_b32_e32 v4, 4, v12
	v_or3_b32 v3, v3, v5, v2
	v_lshlrev_b32_e32 v5, 6, v13
	v_lshl_or_b32 v4, v11, 2, v4
	v_or3_b32 v43, v4, v5, v10
	v_lshlrev_b32_e32 v4, 4, v16
	v_lshlrev_b32_e32 v5, 6, v17
	v_lshl_or_b32 v4, v15, 2, v4
	v_lshlrev_b32_e32 v8, 4, v8
	v_or3_b32 v42, v4, v5, v14
	v_lshlrev_b32_e32 v4, 4, v20
	v_lshlrev_b32_e32 v9, 6, v9
	v_lshl_or_b32 v7, v7, 2, v8
	v_lshlrev_b32_e32 v5, 6, v21
	v_lshl_or_b32 v4, v19, 2, v4
	v_or3_b32 v44, v7, v9, v6
	v_or3_b32 v41, v4, v5, v18
	v_lshlrev_b32_e32 v4, 4, v24
	v_mov_b32_e32 v7, 0
	v_mov_b32_e32 v8, 0x64c
	v_lshlrev_b32_e32 v5, 6, v25
	v_lshl_or_b32 v4, v23, 2, v4
	s_waitcnt lgkmcnt(0)
	s_barrier
	ds_read_b96 v[36:38], v7 offset:1600
	ds_read_b64 v[16:17], v7 offset:1624
	ds_read2_b32 v[20:21], v8 offset1:1
	v_or3_b32 v19, v4, v5, v22
	v_lshlrev_b32_e32 v4, 4, v28
	v_lshlrev_b32_e32 v5, 6, v29
	v_lshl_or_b32 v4, v27, 2, v4
	v_or3_b32 v13, v4, v5, v26
	v_lshlrev_b32_e32 v4, 4, v32
	v_lshlrev_b32_e32 v5, 6, v33
	v_lshl_or_b32 v4, v31, 2, v4
	v_or3_b32 v9, v4, v5, v30
	ds_read_b32 v8, v7 offset:1620
	ds_read_b32 v12, v7 offset:1632
	ds_read_b128 v[30:33], v134 offset:49152
	s_movk_i32 s3, 0xfff
	v_mov_b32_e32 v11, 0x670
	v_mov_b32_e32 v15, 0x10000
	v_mov_b32_e32 v164, 1
	v_mov_b32_e32 v165, 2
	s_mov_b32 s16, 0xfff0fff0
	v_and_b32_e32 v154, 3, v44
	v_bfe_u32 v155, v44, 2, 2
	v_bfe_u32 v156, v44, 4, 2
	v_bfe_u32 v157, v44, 6, 2
	s_waitcnt lgkmcnt(0)
	v_mov_b32_e32 v24, v38
	v_pk_fma_f32 v[22:23], v[76:77], v[20:21], v[16:17] op_sel_hi:[1,0,0]
	v_pk_fma_f32 v[22:23], v[78:79], v[36:37], v[22:23] op_sel_hi:[1,0,1]
	s_nop 0
	v_exp_f32_e32 v26, v22
	v_exp_f32_e32 v27, v23
	v_cmp_eq_u32_e32 vcc, 1, v154
	v_cvt_pknorm_u16_f32 v158, v26, v27
	v_and_b32_e32 v159, s16, v158
	v_cndmask_b32_e32 v162, v164, v15, vcc
	v_cndmask_b32_e32 v150, 0, v26, vcc
	v_cmp_eq_u32_e32 vcc, 1, v155
	v_lshrrev_b32_sdwa v160, v165, v159 dst_sel:DWORD dst_unused:UNUSED_PAD src0_sel:DWORD src1_sel:WORD_0
	v_lshrrev_b32_sdwa v161, v165, v159 dst_sel:DWORD dst_unused:UNUSED_PAD src0_sel:DWORD src1_sel:WORD_1
	v_cndmask_b32_e32 v163, v164, v15, vcc
	v_cndmask_b32_e32 v151, 0, v27, vcc
	ds_add_u32 v160, v162 offset:1648
	ds_add_u32 v161, v163 offset:1648
	v_pk_fma_f32 v[22:23], v[76:77], v[20:21], v[16:17] op_sel:[0,1,1]
	v_pk_fma_f32 v[22:23], v[78:79], v[36:37], v[22:23] op_sel:[0,1,0]
	s_nop 0
	v_exp_f32_e32 v26, v22
	v_exp_f32_e32 v27, v23
	v_cmp_eq_u32_e32 vcc, 2, v154
	v_cvt_pknorm_u16_f32 v158, v26, v27
	v_and_b32_e32 v159, s16, v158
	v_cndmask_b32_e32 v162, v164, v15, vcc
	v_cndmask_b32_e32 v150, v150, v26, vcc
	v_cmp_eq_u32_e32 vcc, 2, v155
	v_lshrrev_b32_sdwa v160, v165, v159 dst_sel:DWORD dst_unused:UNUSED_PAD src0_sel:DWORD src1_sel:WORD_0
	v_lshrrev_b32_sdwa v161, v165, v159 dst_sel:DWORD dst_unused:UNUSED_PAD src0_sel:DWORD src1_sel:WORD_1
	v_cndmask_b32_e32 v163, v164, v15, vcc
	v_cndmask_b32_e32 v151, v151, v27, vcc
	ds_add_u32 v160, v162 offset:18032
	ds_add_u32 v161, v163 offset:18032
	v_pk_fma_f32 v[22:23], v[76:77], v[8:9], v[12:13] op_sel_hi:[1,0,0]
	v_pk_fma_f32 v[22:23], v[78:79], v[24:25], v[22:23] op_sel_hi:[1,0,1]
	s_nop 0
	v_exp_f32_e32 v26, v22
	v_exp_f32_e32 v27, v23
	v_cmp_eq_u32_e32 vcc, 3, v154
	v_cvt_pknorm_u16_f32 v158, v26, v27
	v_and_b32_e32 v159, s16, v158
	v_cndmask_b32_e32 v162, v164, v15, vcc
	v_cndmask_b32_e32 v150, v150, v26, vcc
	v_cmp_eq_u32_e32 vcc, 3, v155
	v_lshrrev_b32_sdwa v160, v165, v159 dst_sel:DWORD dst_unused:UNUSED_PAD src0_sel:DWORD src1_sel:WORD_0
	v_lshrrev_b32_sdwa v161, v165, v159 dst_sel:DWORD dst_unused:UNUSED_PAD src0_sel:DWORD src1_sel:WORD_1
	v_cndmask_b32_e32 v163, v164, v15, vcc
	v_cndmask_b32_e32 v151, v151, v27, vcc
	ds_add_u32 v160, v162 offset:34416
	ds_add_u32 v161, v163 offset:34416
	s_waitcnt lgkmcnt(6)
	v_pk_add_f32 v[166:167], v[30:31], v[150:151] neg_lo:[0,1] neg_hi:[0,1]
	s_nop 0
	v_pk_mul_f32 v[166:167], v[166:167], v[166:167]
	v_pk_fma_f32 v[22:23], v[80:81], v[20:21], v[16:17] op_sel_hi:[1,0,0]
	v_pk_fma_f32 v[22:23], v[82:83], v[36:37], v[22:23] op_sel_hi:[1,0,1]
	s_nop 0
	v_exp_f32_e32 v26, v22
	v_exp_f32_e32 v27, v23
	v_cmp_eq_u32_e32 vcc, 1, v156
	v_cvt_pknorm_u16_f32 v158, v26, v27
	v_and_b32_e32 v159, s16, v158
	v_cndmask_b32_e32 v162, v164, v15, vcc
	v_cndmask_b32_e32 v152, 0, v26, vcc
	v_cmp_eq_u32_e32 vcc, 1, v157
	v_lshrrev_b32_sdwa v160, v165, v159 dst_sel:DWORD dst_unused:UNUSED_PAD src0_sel:DWORD src1_sel:WORD_0
	v_lshrrev_b32_sdwa v161, v165, v159 dst_sel:DWORD dst_unused:UNUSED_PAD src0_sel:DWORD src1_sel:WORD_1
	v_cndmask_b32_e32 v163, v164, v15, vcc
	v_cndmask_b32_e32 v153, 0, v27, vcc
	ds_add_u32 v160, v162 offset:1648
	ds_add_u32 v161, v163 offset:1648
	v_pk_fma_f32 v[22:23], v[80:81], v[20:21], v[16:17] op_sel:[0,1,1]
	v_pk_fma_f32 v[22:23], v[82:83], v[36:37], v[22:23] op_sel:[0,1,0]
	s_nop 0
	v_exp_f32_e32 v26, v22
	v_exp_f32_e32 v27, v23
	v_cmp_eq_u32_e32 vcc, 2, v156
	v_cvt_pknorm_u16_f32 v158, v26, v27
	v_and_b32_e32 v159, s16, v158
	v_cndmask_b32_e32 v162, v164, v15, vcc
	v_cndmask_b32_e32 v152, v152, v26, vcc
	v_cmp_eq_u32_e32 vcc, 2, v157
	v_lshrrev_b32_sdwa v160, v165, v159 dst_sel:DWORD dst_unused:UNUSED_PAD src0_sel:DWORD src1_sel:WORD_0
	v_lshrrev_b32_sdwa v161, v165, v159 dst_sel:DWORD dst_unused:UNUSED_PAD src0_sel:DWORD src1_sel:WORD_1
	v_cndmask_b32_e32 v163, v164, v15, vcc
	v_cndmask_b32_e32 v153, v153, v27, vcc
	ds_add_u32 v160, v162 offset:18032
	ds_add_u32 v161, v163 offset:18032
	v_pk_fma_f32 v[22:23], v[80:81], v[8:9], v[12:13] op_sel_hi:[1,0,0]
	v_pk_fma_f32 v[22:23], v[82:83], v[24:25], v[22:23] op_sel_hi:[1,0,1]
	s_nop 0
	v_exp_f32_e32 v26, v22
	v_exp_f32_e32 v27, v23
	v_cmp_eq_u32_e32 vcc, 3, v156
	v_cvt_pknorm_u16_f32 v158, v26, v27
	v_and_b32_e32 v159, s16, v158
	v_cndmask_b32_e32 v162, v164, v15, vcc
	v_cndmask_b32_e32 v152, v152, v26, vcc
	v_cmp_eq_u32_e32 vcc, 3, v157
	v_lshrrev_b32_sdwa v160, v165, v159 dst_sel:DWORD dst_unused:UNUSED_PAD src0_sel:DWORD src1_sel:WORD_0
	v_lshrrev_b32_sdwa v161, v165, v159 dst_sel:DWORD dst_unused:UNUSED_PAD src0_sel:DWORD src1_sel:WORD_1
	v_cndmask_b32_e32 v163, v164, v15, vcc
	v_cndmask_b32_e32 v153, v153, v27, vcc
	ds_add_u32 v160, v162 offset:34416
	ds_add_u32 v161, v163 offset:34416
	v_pk_add_f32 v[22:23], v[32:33], v[152:153] neg_lo:[0,1] neg_hi:[0,1]
	s_nop 0
	v_pk_fma_f32 v[28:29], v[22:23], v[22:23], v[166:167]
	ds_read_b128 v[76:79], v134 offset:61440
	v_and_b32_e32 v154, 3, v3
	v_bfe_u32 v155, v3, 2, 2
	v_bfe_u32 v156, v3, 4, 2
	v_bfe_u32 v157, v3, 6, 2
	v_pk_fma_f32 v[80:81], v[84:85], v[20:21], v[16:17] op_sel_hi:[1,0,0]
	v_pk_fma_f32 v[80:81], v[86:87], v[36:37], v[80:81] op_sel_hi:[1,0,1]
	s_nop 0
	v_exp_f32_e32 v82, v80
	v_exp_f32_e32 v83, v81
	v_cmp_eq_u32_e32 vcc, 1, v154
	v_cvt_pknorm_u16_f32 v158, v82, v83
	v_and_b32_e32 v159, s16, v158
	v_cndmask_b32_e32 v162, v164, v15, vcc
	v_cndmask_b32_e32 v150, 0, v82, vcc
	v_cmp_eq_u32_e32 vcc, 1, v155
	v_lshrrev_b32_sdwa v160, v165, v159 dst_sel:DWORD dst_unused:UNUSED_PAD src0_sel:DWORD src1_sel:WORD_0
	v_lshrrev_b32_sdwa v161, v165, v159 dst_sel:DWORD dst_unused:UNUSED_PAD src0_sel:DWORD src1_sel:WORD_1
	v_cndmask_b32_e32 v163, v164, v15, vcc
	v_cndmask_b32_e32 v151, 0, v83, vcc
	ds_add_u32 v160, v162 offset:1648
	ds_add_u32 v161, v163 offset:1648
	v_pk_fma_f32 v[80:81], v[84:85], v[20:21], v[16:17] op_sel:[0,1,1]
	v_pk_fma_f32 v[80:81], v[86:87], v[36:37], v[80:81] op_sel:[0,1,0]
	s_nop 0
	v_exp_f32_e32 v82, v80
	v_exp_f32_e32 v83, v81
	v_cmp_eq_u32_e32 vcc, 2, v154
	v_cvt_pknorm_u16_f32 v158, v82, v83
	v_and_b32_e32 v159, s16, v158
	v_cndmask_b32_e32 v162, v164, v15, vcc
	v_cndmask_b32_e32 v150, v150, v82, vcc
	v_cmp_eq_u32_e32 vcc, 2, v155
	v_lshrrev_b32_sdwa v160, v165, v159 dst_sel:DWORD dst_unused:UNUSED_PAD src0_sel:DWORD src1_sel:WORD_0
	v_lshrrev_b32_sdwa v161, v165, v159 dst_sel:DWORD dst_unused:UNUSED_PAD src0_sel:DWORD src1_sel:WORD_1
	v_cndmask_b32_e32 v163, v164, v15, vcc
	v_cndmask_b32_e32 v151, v151, v83, vcc
	ds_add_u32 v160, v162 offset:18032
	ds_add_u32 v161, v163 offset:18032
	v_pk_fma_f32 v[80:81], v[84:85], v[8:9], v[12:13] op_sel_hi:[1,0,0]
	v_pk_fma_f32 v[80:81], v[86:87], v[24:25], v[80:81] op_sel_hi:[1,0,1]
	s_nop 0
	v_exp_f32_e32 v82, v80
	v_exp_f32_e32 v83, v81
	v_cmp_eq_u32_e32 vcc, 3, v154
	v_cvt_pknorm_u16_f32 v158, v82, v83
	v_and_b32_e32 v159, s16, v158
	v_cndmask_b32_e32 v162, v164, v15, vcc
	v_cndmask_b32_e32 v150, v150, v82, vcc
	v_cmp_eq_u32_e32 vcc, 3, v155
	v_lshrrev_b32_sdwa v160, v165, v159 dst_sel:DWORD dst_unused:UNUSED_PAD src0_sel:DWORD src1_sel:WORD_0
	v_lshrrev_b32_sdwa v161, v165, v159 dst_sel:DWORD dst_unused:UNUSED_PAD src0_sel:DWORD src1_sel:WORD_1
	v_cndmask_b32_e32 v163, v164, v15, vcc
	v_cndmask_b32_e32 v151, v151, v83, vcc
	ds_add_u32 v160, v162 offset:34416
	ds_add_u32 v161, v163 offset:34416
	s_waitcnt lgkmcnt(6)
	v_pk_add_f32 v[166:167], v[76:77], v[150:151] neg_lo:[0,1] neg_hi:[0,1]
	s_nop 0
	v_pk_fma_f32 v[166:167], v[166:167], v[166:167], v[28:29]
	v_pk_fma_f32 v[80:81], v[88:89], v[20:21], v[16:17] op_sel_hi:[1,0,0]
	v_pk_fma_f32 v[80:81], v[90:91], v[36:37], v[80:81] op_sel_hi:[1,0,1]
	s_nop 0
	v_exp_f32_e32 v82, v80
	v_exp_f32_e32 v83, v81
	v_cmp_eq_u32_e32 vcc, 1, v156
	v_cvt_pknorm_u16_f32 v158, v82, v83
	v_and_b32_e32 v159, s16, v158
	v_cndmask_b32_e32 v162, v164, v15, vcc
	v_cndmask_b32_e32 v152, 0, v82, vcc
	v_cmp_eq_u32_e32 vcc, 1, v157
	v_lshrrev_b32_sdwa v160, v165, v159 dst_sel:DWORD dst_unused:UNUSED_PAD src0_sel:DWORD src1_sel:WORD_0
	v_lshrrev_b32_sdwa v161, v165, v159 dst_sel:DWORD dst_unused:UNUSED_PAD src0_sel:DWORD src1_sel:WORD_1
	v_cndmask_b32_e32 v163, v164, v15, vcc
	v_cndmask_b32_e32 v153, 0, v83, vcc
	ds_add_u32 v160, v162 offset:1648
	ds_add_u32 v161, v163 offset:1648
	v_pk_fma_f32 v[80:81], v[88:89], v[20:21], v[16:17] op_sel:[0,1,1]
	v_pk_fma_f32 v[80:81], v[90:91], v[36:37], v[80:81] op_sel:[0,1,0]
	s_nop 0
	v_exp_f32_e32 v82, v80
	v_exp_f32_e32 v83, v81
	v_cmp_eq_u32_e32 vcc, 2, v156
	v_cvt_pknorm_u16_f32 v158, v82, v83
	v_and_b32_e32 v159, s16, v158
	v_cndmask_b32_e32 v162, v164, v15, vcc
	v_cndmask_b32_e32 v152, v152, v82, vcc
	v_cmp_eq_u32_e32 vcc, 2, v157
	v_lshrrev_b32_sdwa v160, v165, v159 dst_sel:DWORD dst_unused:UNUSED_PAD src0_sel:DWORD src1_sel:WORD_0
	v_lshrrev_b32_sdwa v161, v165, v159 dst_sel:DWORD dst_unused:UNUSED_PAD src0_sel:DWORD src1_sel:WORD_1
	v_cndmask_b32_e32 v163, v164, v15, vcc
	v_cndmask_b32_e32 v153, v153, v83, vcc
	ds_add_u32 v160, v162 offset:18032
	ds_add_u32 v161, v163 offset:18032
	v_pk_fma_f32 v[80:81], v[88:89], v[8:9], v[12:13] op_sel_hi:[1,0,0]
	v_pk_fma_f32 v[80:81], v[90:91], v[24:25], v[80:81] op_sel_hi:[1,0,1]
	s_nop 0
	v_exp_f32_e32 v82, v80
	v_exp_f32_e32 v83, v81
	v_cmp_eq_u32_e32 vcc, 3, v156
	v_cvt_pknorm_u16_f32 v158, v82, v83
	v_and_b32_e32 v159, s16, v158
	v_cndmask_b32_e32 v162, v164, v15, vcc
	v_cndmask_b32_e32 v152, v152, v82, vcc
	v_cmp_eq_u32_e32 vcc, 3, v157
	v_lshrrev_b32_sdwa v160, v165, v159 dst_sel:DWORD dst_unused:UNUSED_PAD src0_sel:DWORD src1_sel:WORD_0
	v_lshrrev_b32_sdwa v161, v165, v159 dst_sel:DWORD dst_unused:UNUSED_PAD src0_sel:DWORD src1_sel:WORD_1
	v_cndmask_b32_e32 v163, v164, v15, vcc
	v_cndmask_b32_e32 v153, v153, v83, vcc
	ds_add_u32 v160, v162 offset:34416
	ds_add_u32 v161, v163 offset:34416
	v_pk_add_f32 v[80:81], v[78:79], v[152:153] neg_lo:[0,1] neg_hi:[0,1]
	s_nop 0
	v_pk_fma_f32 v[6:7], v[80:81], v[80:81], v[166:167]
	ds_read_b128 v[76:79], v1 offset:24576
	v_and_b32_e32 v154, 3, v43
	v_bfe_u32 v155, v43, 2, 2
	v_bfe_u32 v156, v43, 4, 2
	v_bfe_u32 v157, v43, 6, 2
	v_pk_fma_f32 v[80:81], v[92:93], v[20:21], v[16:17] op_sel_hi:[1,0,0]
	v_pk_fma_f32 v[80:81], v[94:95], v[36:37], v[80:81] op_sel_hi:[1,0,1]
	s_nop 0
	v_exp_f32_e32 v82, v80
	v_exp_f32_e32 v83, v81
	v_cmp_eq_u32_e32 vcc, 1, v154
	v_cvt_pknorm_u16_f32 v158, v82, v83
	v_and_b32_e32 v159, s16, v158
	v_cndmask_b32_e32 v162, v164, v15, vcc
	v_cndmask_b32_e32 v150, 0, v82, vcc
	v_cmp_eq_u32_e32 vcc, 1, v155
	v_lshrrev_b32_sdwa v160, v165, v159 dst_sel:DWORD dst_unused:UNUSED_PAD src0_sel:DWORD src1_sel:WORD_0
	v_lshrrev_b32_sdwa v161, v165, v159 dst_sel:DWORD dst_unused:UNUSED_PAD src0_sel:DWORD src1_sel:WORD_1
	v_cndmask_b32_e32 v163, v164, v15, vcc
	v_cndmask_b32_e32 v151, 0, v83, vcc
	ds_add_u32 v160, v162 offset:1648
	ds_add_u32 v161, v163 offset:1648
	v_pk_fma_f32 v[80:81], v[92:93], v[20:21], v[16:17] op_sel:[0,1,1]
	v_pk_fma_f32 v[80:81], v[94:95], v[36:37], v[80:81] op_sel:[0,1,0]
	s_nop 0
	v_exp_f32_e32 v82, v80
	v_exp_f32_e32 v83, v81
	v_cmp_eq_u32_e32 vcc, 2, v154
	v_cvt_pknorm_u16_f32 v158, v82, v83
	v_and_b32_e32 v159, s16, v158
	v_cndmask_b32_e32 v162, v164, v15, vcc
	v_cndmask_b32_e32 v150, v150, v82, vcc
	v_cmp_eq_u32_e32 vcc, 2, v155
	v_lshrrev_b32_sdwa v160, v165, v159 dst_sel:DWORD dst_unused:UNUSED_PAD src0_sel:DWORD src1_sel:WORD_0
	v_lshrrev_b32_sdwa v161, v165, v159 dst_sel:DWORD dst_unused:UNUSED_PAD src0_sel:DWORD src1_sel:WORD_1
	v_cndmask_b32_e32 v163, v164, v15, vcc
	v_cndmask_b32_e32 v151, v151, v83, vcc
	ds_add_u32 v160, v162 offset:18032
	ds_add_u32 v161, v163 offset:18032
	v_pk_fma_f32 v[80:81], v[92:93], v[8:9], v[12:13] op_sel_hi:[1,0,0]
	v_pk_fma_f32 v[80:81], v[94:95], v[24:25], v[80:81] op_sel_hi:[1,0,1]
	s_nop 0
	v_exp_f32_e32 v82, v80
	v_exp_f32_e32 v83, v81
	v_cmp_eq_u32_e32 vcc, 3, v154
	v_cvt_pknorm_u16_f32 v158, v82, v83
	v_and_b32_e32 v159, s16, v158
	v_cndmask_b32_e32 v162, v164, v15, vcc
	v_cndmask_b32_e32 v150, v150, v82, vcc
	v_cmp_eq_u32_e32 vcc, 3, v155
	v_lshrrev_b32_sdwa v160, v165, v159 dst_sel:DWORD dst_unused:UNUSED_PAD src0_sel:DWORD src1_sel:WORD_0
	v_lshrrev_b32_sdwa v161, v165, v159 dst_sel:DWORD dst_unused:UNUSED_PAD src0_sel:DWORD src1_sel:WORD_1
	v_cndmask_b32_e32 v163, v164, v15, vcc
	v_cndmask_b32_e32 v151, v151, v83, vcc
	ds_add_u32 v160, v162 offset:34416
	ds_add_u32 v161, v163 offset:34416
	s_waitcnt lgkmcnt(6)
	v_pk_add_f32 v[166:167], v[76:77], v[150:151] neg_lo:[0,1] neg_hi:[0,1]
	s_nop 0
	v_pk_fma_f32 v[166:167], v[166:167], v[166:167], v[6:7]
	v_pk_fma_f32 v[80:81], v[96:97], v[20:21], v[16:17] op_sel_hi:[1,0,0]
	v_pk_fma_f32 v[80:81], v[98:99], v[36:37], v[80:81] op_sel_hi:[1,0,1]
	s_nop 0
	v_exp_f32_e32 v82, v80
	v_exp_f32_e32 v83, v81
	v_cmp_eq_u32_e32 vcc, 1, v156
	v_cvt_pknorm_u16_f32 v158, v82, v83
	v_and_b32_e32 v159, s16, v158
	v_cndmask_b32_e32 v162, v164, v15, vcc
	v_cndmask_b32_e32 v152, 0, v82, vcc
	v_cmp_eq_u32_e32 vcc, 1, v157
	v_lshrrev_b32_sdwa v160, v165, v159 dst_sel:DWORD dst_unused:UNUSED_PAD src0_sel:DWORD src1_sel:WORD_0
	v_lshrrev_b32_sdwa v161, v165, v159 dst_sel:DWORD dst_unused:UNUSED_PAD src0_sel:DWORD src1_sel:WORD_1
	v_cndmask_b32_e32 v163, v164, v15, vcc
	v_cndmask_b32_e32 v153, 0, v83, vcc
	ds_add_u32 v160, v162 offset:1648
	ds_add_u32 v161, v163 offset:1648
	v_pk_fma_f32 v[80:81], v[96:97], v[20:21], v[16:17] op_sel:[0,1,1]
	v_pk_fma_f32 v[80:81], v[98:99], v[36:37], v[80:81] op_sel:[0,1,0]
	s_nop 0
	v_exp_f32_e32 v82, v80
	v_exp_f32_e32 v83, v81
	v_cmp_eq_u32_e32 vcc, 2, v156
	v_cvt_pknorm_u16_f32 v158, v82, v83
	v_and_b32_e32 v159, s16, v158
	v_cndmask_b32_e32 v162, v164, v15, vcc
	v_cndmask_b32_e32 v152, v152, v82, vcc
	v_cmp_eq_u32_e32 vcc, 2, v157
	v_lshrrev_b32_sdwa v160, v165, v159 dst_sel:DWORD dst_unused:UNUSED_PAD src0_sel:DWORD src1_sel:WORD_0
	v_lshrrev_b32_sdwa v161, v165, v159 dst_sel:DWORD dst_unused:UNUSED_PAD src0_sel:DWORD src1_sel:WORD_1
	v_cndmask_b32_e32 v163, v164, v15, vcc
	v_cndmask_b32_e32 v153, v153, v83, vcc
	ds_add_u32 v160, v162 offset:18032
	ds_add_u32 v161, v163 offset:18032
	v_pk_fma_f32 v[80:81], v[96:97], v[8:9], v[12:13] op_sel_hi:[1,0,0]
	v_pk_fma_f32 v[80:81], v[98:99], v[24:25], v[80:81] op_sel_hi:[1,0,1]
	s_nop 0
	v_exp_f32_e32 v82, v80
	v_exp_f32_e32 v83, v81
	v_cmp_eq_u32_e32 vcc, 3, v156
	v_cvt_pknorm_u16_f32 v158, v82, v83
	v_and_b32_e32 v159, s16, v158
	v_cndmask_b32_e32 v162, v164, v15, vcc
	v_cndmask_b32_e32 v152, v152, v82, vcc
	v_cmp_eq_u32_e32 vcc, 3, v157
	v_lshrrev_b32_sdwa v160, v165, v159 dst_sel:DWORD dst_unused:UNUSED_PAD src0_sel:DWORD src1_sel:WORD_0
	v_lshrrev_b32_sdwa v161, v165, v159 dst_sel:DWORD dst_unused:UNUSED_PAD src0_sel:DWORD src1_sel:WORD_1
	v_cndmask_b32_e32 v163, v164, v15, vcc
	v_cndmask_b32_e32 v153, v153, v83, vcc
	ds_add_u32 v160, v162 offset:34416
	ds_add_u32 v161, v163 offset:34416
	v_pk_add_f32 v[80:81], v[78:79], v[152:153] neg_lo:[0,1] neg_hi:[0,1]
	s_nop 0
	v_pk_fma_f32 v[6:7], v[80:81], v[80:81], v[166:167]
	ds_read_b128 v[76:79], v1 offset:36864
	v_and_b32_e32 v154, 3, v42
	v_bfe_u32 v155, v42, 2, 2
	v_bfe_u32 v156, v42, 4, 2
	v_bfe_u32 v157, v42, 6, 2
	v_pk_fma_f32 v[80:81], v[100:101], v[20:21], v[16:17] op_sel_hi:[1,0,0]
	v_pk_fma_f32 v[80:81], v[102:103], v[36:37], v[80:81] op_sel_hi:[1,0,1]
	s_nop 0
	v_exp_f32_e32 v82, v80
	v_exp_f32_e32 v83, v81
	v_cmp_eq_u32_e32 vcc, 1, v154
	v_cvt_pknorm_u16_f32 v158, v82, v83
	v_and_b32_e32 v159, s16, v158
	v_cndmask_b32_e32 v162, v164, v15, vcc
	v_cndmask_b32_e32 v150, 0, v82, vcc
	v_cmp_eq_u32_e32 vcc, 1, v155
	v_lshrrev_b32_sdwa v160, v165, v159 dst_sel:DWORD dst_unused:UNUSED_PAD src0_sel:DWORD src1_sel:WORD_0
	v_lshrrev_b32_sdwa v161, v165, v159 dst_sel:DWORD dst_unused:UNUSED_PAD src0_sel:DWORD src1_sel:WORD_1
	v_cndmask_b32_e32 v163, v164, v15, vcc
	v_cndmask_b32_e32 v151, 0, v83, vcc
	ds_add_u32 v160, v162 offset:1648
	ds_add_u32 v161, v163 offset:1648
	v_pk_fma_f32 v[80:81], v[100:101], v[20:21], v[16:17] op_sel:[0,1,1]
	v_pk_fma_f32 v[80:81], v[102:103], v[36:37], v[80:81] op_sel:[0,1,0]
	s_nop 0
	v_exp_f32_e32 v82, v80
	v_exp_f32_e32 v83, v81
	v_cmp_eq_u32_e32 vcc, 2, v154
	v_cvt_pknorm_u16_f32 v158, v82, v83
	v_and_b32_e32 v159, s16, v158
	v_cndmask_b32_e32 v162, v164, v15, vcc
	v_cndmask_b32_e32 v150, v150, v82, vcc
	v_cmp_eq_u32_e32 vcc, 2, v155
	v_lshrrev_b32_sdwa v160, v165, v159 dst_sel:DWORD dst_unused:UNUSED_PAD src0_sel:DWORD src1_sel:WORD_0
	v_lshrrev_b32_sdwa v161, v165, v159 dst_sel:DWORD dst_unused:UNUSED_PAD src0_sel:DWORD src1_sel:WORD_1
	v_cndmask_b32_e32 v163, v164, v15, vcc
	v_cndmask_b32_e32 v151, v151, v83, vcc
	ds_add_u32 v160, v162 offset:18032
	ds_add_u32 v161, v163 offset:18032
	v_pk_fma_f32 v[80:81], v[100:101], v[8:9], v[12:13] op_sel_hi:[1,0,0]
	v_pk_fma_f32 v[80:81], v[102:103], v[24:25], v[80:81] op_sel_hi:[1,0,1]
	s_nop 0
	v_exp_f32_e32 v82, v80
	v_exp_f32_e32 v83, v81
	v_cmp_eq_u32_e32 vcc, 3, v154
	v_cvt_pknorm_u16_f32 v158, v82, v83
	v_and_b32_e32 v159, s16, v158
	v_cndmask_b32_e32 v162, v164, v15, vcc
	v_cndmask_b32_e32 v150, v150, v82, vcc
	v_cmp_eq_u32_e32 vcc, 3, v155
	v_lshrrev_b32_sdwa v160, v165, v159 dst_sel:DWORD dst_unused:UNUSED_PAD src0_sel:DWORD src1_sel:WORD_0
	v_lshrrev_b32_sdwa v161, v165, v159 dst_sel:DWORD dst_unused:UNUSED_PAD src0_sel:DWORD src1_sel:WORD_1
	v_cndmask_b32_e32 v163, v164, v15, vcc
	v_cndmask_b32_e32 v151, v151, v83, vcc
	ds_add_u32 v160, v162 offset:34416
	ds_add_u32 v161, v163 offset:34416
	s_waitcnt lgkmcnt(6)
	v_pk_add_f32 v[166:167], v[76:77], v[150:151] neg_lo:[0,1] neg_hi:[0,1]
	s_nop 0
	v_pk_fma_f32 v[166:167], v[166:167], v[166:167], v[6:7]
	v_pk_fma_f32 v[80:81], v[104:105], v[20:21], v[16:17] op_sel_hi:[1,0,0]
	v_pk_fma_f32 v[80:81], v[106:107], v[36:37], v[80:81] op_sel_hi:[1,0,1]
	s_nop 0
	v_exp_f32_e32 v82, v80
	v_exp_f32_e32 v83, v81
	v_cmp_eq_u32_e32 vcc, 1, v156
	v_cvt_pknorm_u16_f32 v158, v82, v83
	v_and_b32_e32 v159, s16, v158
	v_cndmask_b32_e32 v162, v164, v15, vcc
	v_cndmask_b32_e32 v152, 0, v82, vcc
	v_cmp_eq_u32_e32 vcc, 1, v157
	v_lshrrev_b32_sdwa v160, v165, v159 dst_sel:DWORD dst_unused:UNUSED_PAD src0_sel:DWORD src1_sel:WORD_0
	v_lshrrev_b32_sdwa v161, v165, v159 dst_sel:DWORD dst_unused:UNUSED_PAD src0_sel:DWORD src1_sel:WORD_1
	v_cndmask_b32_e32 v163, v164, v15, vcc
	v_cndmask_b32_e32 v153, 0, v83, vcc
	ds_add_u32 v160, v162 offset:1648
	ds_add_u32 v161, v163 offset:1648
	v_pk_fma_f32 v[80:81], v[104:105], v[20:21], v[16:17] op_sel:[0,1,1]
	v_pk_fma_f32 v[80:81], v[106:107], v[36:37], v[80:81] op_sel:[0,1,0]
	s_nop 0
	v_exp_f32_e32 v82, v80
	v_exp_f32_e32 v83, v81
	v_cmp_eq_u32_e32 vcc, 2, v156
	v_cvt_pknorm_u16_f32 v158, v82, v83
	v_and_b32_e32 v159, s16, v158
	v_cndmask_b32_e32 v162, v164, v15, vcc
	v_cndmask_b32_e32 v152, v152, v82, vcc
	v_cmp_eq_u32_e32 vcc, 2, v157
	v_lshrrev_b32_sdwa v160, v165, v159 dst_sel:DWORD dst_unused:UNUSED_PAD src0_sel:DWORD src1_sel:WORD_0
	v_lshrrev_b32_sdwa v161, v165, v159 dst_sel:DWORD dst_unused:UNUSED_PAD src0_sel:DWORD src1_sel:WORD_1
	v_cndmask_b32_e32 v163, v164, v15, vcc
	v_cndmask_b32_e32 v153, v153, v83, vcc
	ds_add_u32 v160, v162 offset:18032
	ds_add_u32 v161, v163 offset:18032
	v_pk_fma_f32 v[80:81], v[104:105], v[8:9], v[12:13] op_sel_hi:[1,0,0]
	v_pk_fma_f32 v[80:81], v[106:107], v[24:25], v[80:81] op_sel_hi:[1,0,1]
	s_nop 0
	v_exp_f32_e32 v82, v80
	v_exp_f32_e32 v83, v81
	v_cmp_eq_u32_e32 vcc, 3, v156
	v_cvt_pknorm_u16_f32 v158, v82, v83
	v_and_b32_e32 v159, s16, v158
	v_cndmask_b32_e32 v162, v164, v15, vcc
	v_cndmask_b32_e32 v152, v152, v82, vcc
	v_cmp_eq_u32_e32 vcc, 3, v157
	v_lshrrev_b32_sdwa v160, v165, v159 dst_sel:DWORD dst_unused:UNUSED_PAD src0_sel:DWORD src1_sel:WORD_0
	v_lshrrev_b32_sdwa v161, v165, v159 dst_sel:DWORD dst_unused:UNUSED_PAD src0_sel:DWORD src1_sel:WORD_1
	v_cndmask_b32_e32 v163, v164, v15, vcc
	v_cndmask_b32_e32 v153, v153, v83, vcc
	ds_add_u32 v160, v162 offset:34416
	ds_add_u32 v161, v163 offset:34416
	v_pk_add_f32 v[80:81], v[78:79], v[152:153] neg_lo:[0,1] neg_hi:[0,1]
	s_nop 0
	v_pk_fma_f32 v[6:7], v[80:81], v[80:81], v[166:167]
	ds_read_b128 v[76:79], v1 offset:49152
	v_and_b32_e32 v154, 3, v41
	v_bfe_u32 v155, v41, 2, 2
	v_bfe_u32 v156, v41, 4, 2
	v_bfe_u32 v157, v41, 6, 2
	v_pk_fma_f32 v[80:81], v[108:109], v[20:21], v[16:17] op_sel_hi:[1,0,0]
	v_pk_fma_f32 v[80:81], v[110:111], v[36:37], v[80:81] op_sel_hi:[1,0,1]
	s_nop 0
	v_exp_f32_e32 v82, v80
	v_exp_f32_e32 v83, v81
	v_cmp_eq_u32_e32 vcc, 1, v154
	v_cvt_pknorm_u16_f32 v158, v82, v83
	v_and_b32_e32 v159, s16, v158
	v_cndmask_b32_e32 v162, v164, v15, vcc
	v_cndmask_b32_e32 v150, 0, v82, vcc
	v_cmp_eq_u32_e32 vcc, 1, v155
	v_lshrrev_b32_sdwa v160, v165, v159 dst_sel:DWORD dst_unused:UNUSED_PAD src0_sel:DWORD src1_sel:WORD_0
	v_lshrrev_b32_sdwa v161, v165, v159 dst_sel:DWORD dst_unused:UNUSED_PAD src0_sel:DWORD src1_sel:WORD_1
	v_cndmask_b32_e32 v163, v164, v15, vcc
	v_cndmask_b32_e32 v151, 0, v83, vcc
	ds_add_u32 v160, v162 offset:1648
	ds_add_u32 v161, v163 offset:1648
	v_pk_fma_f32 v[80:81], v[108:109], v[20:21], v[16:17] op_sel:[0,1,1]
	v_pk_fma_f32 v[80:81], v[110:111], v[36:37], v[80:81] op_sel:[0,1,0]
	s_nop 0
	v_exp_f32_e32 v82, v80
	v_exp_f32_e32 v83, v81
	v_cmp_eq_u32_e32 vcc, 2, v154
	v_cvt_pknorm_u16_f32 v158, v82, v83
	v_and_b32_e32 v159, s16, v158
	v_cndmask_b32_e32 v162, v164, v15, vcc
	v_cndmask_b32_e32 v150, v150, v82, vcc
	v_cmp_eq_u32_e32 vcc, 2, v155
	v_lshrrev_b32_sdwa v160, v165, v159 dst_sel:DWORD dst_unused:UNUSED_PAD src0_sel:DWORD src1_sel:WORD_0
	v_lshrrev_b32_sdwa v161, v165, v159 dst_sel:DWORD dst_unused:UNUSED_PAD src0_sel:DWORD src1_sel:WORD_1
	v_cndmask_b32_e32 v163, v164, v15, vcc
	v_cndmask_b32_e32 v151, v151, v83, vcc
	ds_add_u32 v160, v162 offset:18032
	ds_add_u32 v161, v163 offset:18032
	v_pk_fma_f32 v[80:81], v[108:109], v[8:9], v[12:13] op_sel_hi:[1,0,0]
	v_pk_fma_f32 v[80:81], v[110:111], v[24:25], v[80:81] op_sel_hi:[1,0,1]
	s_nop 0
	v_exp_f32_e32 v82, v80
	v_exp_f32_e32 v83, v81
	v_cmp_eq_u32_e32 vcc, 3, v154
	v_cvt_pknorm_u16_f32 v158, v82, v83
	v_and_b32_e32 v159, s16, v158
	v_cndmask_b32_e32 v162, v164, v15, vcc
	v_cndmask_b32_e32 v150, v150, v82, vcc
	v_cmp_eq_u32_e32 vcc, 3, v155
	v_lshrrev_b32_sdwa v160, v165, v159 dst_sel:DWORD dst_unused:UNUSED_PAD src0_sel:DWORD src1_sel:WORD_0
	v_lshrrev_b32_sdwa v161, v165, v159 dst_sel:DWORD dst_unused:UNUSED_PAD src0_sel:DWORD src1_sel:WORD_1
	v_cndmask_b32_e32 v163, v164, v15, vcc
	v_cndmask_b32_e32 v151, v151, v83, vcc
	ds_add_u32 v160, v162 offset:34416
	ds_add_u32 v161, v163 offset:34416
	s_waitcnt lgkmcnt(6)
	v_pk_add_f32 v[166:167], v[76:77], v[150:151] neg_lo:[0,1] neg_hi:[0,1]
	s_nop 0
	v_pk_fma_f32 v[166:167], v[166:167], v[166:167], v[6:7]
	v_pk_fma_f32 v[80:81], v[112:113], v[20:21], v[16:17] op_sel_hi:[1,0,0]
	v_pk_fma_f32 v[80:81], v[114:115], v[36:37], v[80:81] op_sel_hi:[1,0,1]
	s_nop 0
	v_exp_f32_e32 v82, v80
	v_exp_f32_e32 v83, v81
	v_cmp_eq_u32_e32 vcc, 1, v156
	v_cvt_pknorm_u16_f32 v158, v82, v83
	v_and_b32_e32 v159, s16, v158
	v_cndmask_b32_e32 v162, v164, v15, vcc
	v_cndmask_b32_e32 v152, 0, v82, vcc
	v_cmp_eq_u32_e32 vcc, 1, v157
	v_lshrrev_b32_sdwa v160, v165, v159 dst_sel:DWORD dst_unused:UNUSED_PAD src0_sel:DWORD src1_sel:WORD_0
	v_lshrrev_b32_sdwa v161, v165, v159 dst_sel:DWORD dst_unused:UNUSED_PAD src0_sel:DWORD src1_sel:WORD_1
	v_cndmask_b32_e32 v163, v164, v15, vcc
	v_cndmask_b32_e32 v153, 0, v83, vcc
	ds_add_u32 v160, v162 offset:1648
	ds_add_u32 v161, v163 offset:1648
	v_pk_fma_f32 v[80:81], v[112:113], v[20:21], v[16:17] op_sel:[0,1,1]
	v_pk_fma_f32 v[80:81], v[114:115], v[36:37], v[80:81] op_sel:[0,1,0]
	s_nop 0
	v_exp_f32_e32 v82, v80
	v_exp_f32_e32 v83, v81
	v_cmp_eq_u32_e32 vcc, 2, v156
	v_cvt_pknorm_u16_f32 v158, v82, v83
	v_and_b32_e32 v159, s16, v158
	v_cndmask_b32_e32 v162, v164, v15, vcc
	v_cndmask_b32_e32 v152, v152, v82, vcc
	v_cmp_eq_u32_e32 vcc, 2, v157
	v_lshrrev_b32_sdwa v160, v165, v159 dst_sel:DWORD dst_unused:UNUSED_PAD src0_sel:DWORD src1_sel:WORD_0
	v_lshrrev_b32_sdwa v161, v165, v159 dst_sel:DWORD dst_unused:UNUSED_PAD src0_sel:DWORD src1_sel:WORD_1
	v_cndmask_b32_e32 v163, v164, v15, vcc
	v_cndmask_b32_e32 v153, v153, v83, vcc
	ds_add_u32 v160, v162 offset:18032
	ds_add_u32 v161, v163 offset:18032
	v_pk_fma_f32 v[80:81], v[112:113], v[8:9], v[12:13] op_sel_hi:[1,0,0]
	v_pk_fma_f32 v[80:81], v[114:115], v[24:25], v[80:81] op_sel_hi:[1,0,1]
	s_nop 0
	v_exp_f32_e32 v82, v80
	v_exp_f32_e32 v83, v81
	v_cmp_eq_u32_e32 vcc, 3, v156
	v_cvt_pknorm_u16_f32 v158, v82, v83
	v_and_b32_e32 v159, s16, v158
	v_cndmask_b32_e32 v162, v164, v15, vcc
	v_cndmask_b32_e32 v152, v152, v82, vcc
	v_cmp_eq_u32_e32 vcc, 3, v157
	v_lshrrev_b32_sdwa v160, v165, v159 dst_sel:DWORD dst_unused:UNUSED_PAD src0_sel:DWORD src1_sel:WORD_0
	v_lshrrev_b32_sdwa v161, v165, v159 dst_sel:DWORD dst_unused:UNUSED_PAD src0_sel:DWORD src1_sel:WORD_1
	v_cndmask_b32_e32 v163, v164, v15, vcc
	v_cndmask_b32_e32 v153, v153, v83, vcc
	ds_add_u32 v160, v162 offset:34416
	ds_add_u32 v161, v163 offset:34416
	v_pk_add_f32 v[80:81], v[78:79], v[152:153] neg_lo:[0,1] neg_hi:[0,1]
	s_nop 0
	v_pk_fma_f32 v[6:7], v[80:81], v[80:81], v[166:167]
	ds_read_b128 v[76:79], v1 offset:61440
	v_and_b32_e32 v154, 3, v19
	v_bfe_u32 v155, v19, 2, 2
	v_bfe_u32 v156, v19, 4, 2
	v_bfe_u32 v157, v19, 6, 2
	v_pk_fma_f32 v[80:81], v[116:117], v[20:21], v[16:17] op_sel_hi:[1,0,0]
	v_pk_fma_f32 v[80:81], v[118:119], v[36:37], v[80:81] op_sel_hi:[1,0,1]
	s_nop 0
	v_exp_f32_e32 v82, v80
	v_exp_f32_e32 v83, v81
	v_cmp_eq_u32_e32 vcc, 1, v154
	v_cvt_pknorm_u16_f32 v158, v82, v83
	v_and_b32_e32 v159, s16, v158
	v_cndmask_b32_e32 v162, v164, v15, vcc
	v_cndmask_b32_e32 v150, 0, v82, vcc
	v_cmp_eq_u32_e32 vcc, 1, v155
	v_lshrrev_b32_sdwa v160, v165, v159 dst_sel:DWORD dst_unused:UNUSED_PAD src0_sel:DWORD src1_sel:WORD_0
	v_lshrrev_b32_sdwa v161, v165, v159 dst_sel:DWORD dst_unused:UNUSED_PAD src0_sel:DWORD src1_sel:WORD_1
	v_cndmask_b32_e32 v163, v164, v15, vcc
	v_cndmask_b32_e32 v151, 0, v83, vcc
	ds_add_u32 v160, v162 offset:1648
	ds_add_u32 v161, v163 offset:1648
	v_pk_fma_f32 v[80:81], v[116:117], v[20:21], v[16:17] op_sel:[0,1,1]
	v_pk_fma_f32 v[80:81], v[118:119], v[36:37], v[80:81] op_sel:[0,1,0]
	s_nop 0
	v_exp_f32_e32 v82, v80
	v_exp_f32_e32 v83, v81
	v_cmp_eq_u32_e32 vcc, 2, v154
	v_cvt_pknorm_u16_f32 v158, v82, v83
	v_and_b32_e32 v159, s16, v158
	v_cndmask_b32_e32 v162, v164, v15, vcc
	v_cndmask_b32_e32 v150, v150, v82, vcc
	v_cmp_eq_u32_e32 vcc, 2, v155
	v_lshrrev_b32_sdwa v160, v165, v159 dst_sel:DWORD dst_unused:UNUSED_PAD src0_sel:DWORD src1_sel:WORD_0
	v_lshrrev_b32_sdwa v161, v165, v159 dst_sel:DWORD dst_unused:UNUSED_PAD src0_sel:DWORD src1_sel:WORD_1
	v_cndmask_b32_e32 v163, v164, v15, vcc
	v_cndmask_b32_e32 v151, v151, v83, vcc
	ds_add_u32 v160, v162 offset:18032
	ds_add_u32 v161, v163 offset:18032
	v_pk_fma_f32 v[80:81], v[116:117], v[8:9], v[12:13] op_sel_hi:[1,0,0]
	v_pk_fma_f32 v[80:81], v[118:119], v[24:25], v[80:81] op_sel_hi:[1,0,1]
	s_nop 0
	v_exp_f32_e32 v82, v80
	v_exp_f32_e32 v83, v81
	v_cmp_eq_u32_e32 vcc, 3, v154
	v_cvt_pknorm_u16_f32 v158, v82, v83
	v_and_b32_e32 v159, s16, v158
	v_cndmask_b32_e32 v162, v164, v15, vcc
	v_cndmask_b32_e32 v150, v150, v82, vcc
	v_cmp_eq_u32_e32 vcc, 3, v155
	v_lshrrev_b32_sdwa v160, v165, v159 dst_sel:DWORD dst_unused:UNUSED_PAD src0_sel:DWORD src1_sel:WORD_0
	v_lshrrev_b32_sdwa v161, v165, v159 dst_sel:DWORD dst_unused:UNUSED_PAD src0_sel:DWORD src1_sel:WORD_1
	v_cndmask_b32_e32 v163, v164, v15, vcc
	v_cndmask_b32_e32 v151, v151, v83, vcc
	ds_add_u32 v160, v162 offset:34416
	ds_add_u32 v161, v163 offset:34416
	s_waitcnt lgkmcnt(6)
	v_pk_add_f32 v[166:167], v[76:77], v[150:151] neg_lo:[0,1] neg_hi:[0,1]
	s_nop 0
	v_pk_fma_f32 v[166:167], v[166:167], v[166:167], v[6:7]
	v_pk_fma_f32 v[80:81], v[120:121], v[20:21], v[16:17] op_sel_hi:[1,0,0]
	v_pk_fma_f32 v[80:81], v[122:123], v[36:37], v[80:81] op_sel_hi:[1,0,1]
	s_nop 0
	v_exp_f32_e32 v82, v80
	v_exp_f32_e32 v83, v81
	v_cmp_eq_u32_e32 vcc, 1, v156
	v_cvt_pknorm_u16_f32 v158, v82, v83
	v_and_b32_e32 v159, s16, v158
	v_cndmask_b32_e32 v162, v164, v15, vcc
	v_cndmask_b32_e32 v152, 0, v82, vcc
	v_cmp_eq_u32_e32 vcc, 1, v157
	v_lshrrev_b32_sdwa v160, v165, v159 dst_sel:DWORD dst_unused:UNUSED_PAD src0_sel:DWORD src1_sel:WORD_0
	v_lshrrev_b32_sdwa v161, v165, v159 dst_sel:DWORD dst_unused:UNUSED_PAD src0_sel:DWORD src1_sel:WORD_1
	v_cndmask_b32_e32 v163, v164, v15, vcc
	v_cndmask_b32_e32 v153, 0, v83, vcc
	ds_add_u32 v160, v162 offset:1648
	ds_add_u32 v161, v163 offset:1648
	v_pk_fma_f32 v[80:81], v[120:121], v[20:21], v[16:17] op_sel:[0,1,1]
	v_pk_fma_f32 v[80:81], v[122:123], v[36:37], v[80:81] op_sel:[0,1,0]
	s_nop 0
	v_exp_f32_e32 v82, v80
	v_exp_f32_e32 v83, v81
	v_cmp_eq_u32_e32 vcc, 2, v156
	v_cvt_pknorm_u16_f32 v158, v82, v83
	v_and_b32_e32 v159, s16, v158
	v_cndmask_b32_e32 v162, v164, v15, vcc
	v_cndmask_b32_e32 v152, v152, v82, vcc
	v_cmp_eq_u32_e32 vcc, 2, v157
	v_lshrrev_b32_sdwa v160, v165, v159 dst_sel:DWORD dst_unused:UNUSED_PAD src0_sel:DWORD src1_sel:WORD_0
	v_lshrrev_b32_sdwa v161, v165, v159 dst_sel:DWORD dst_unused:UNUSED_PAD src0_sel:DWORD src1_sel:WORD_1
	v_cndmask_b32_e32 v163, v164, v15, vcc
	v_cndmask_b32_e32 v153, v153, v83, vcc
	ds_add_u32 v160, v162 offset:18032
	ds_add_u32 v161, v163 offset:18032
	v_pk_fma_f32 v[80:81], v[120:121], v[8:9], v[12:13] op_sel_hi:[1,0,0]
	v_pk_fma_f32 v[80:81], v[122:123], v[24:25], v[80:81] op_sel_hi:[1,0,1]
	s_nop 0
	v_exp_f32_e32 v82, v80
	v_exp_f32_e32 v83, v81
	v_cmp_eq_u32_e32 vcc, 3, v156
	v_cvt_pknorm_u16_f32 v158, v82, v83
	v_and_b32_e32 v159, s16, v158
	v_cndmask_b32_e32 v162, v164, v15, vcc
	v_cndmask_b32_e32 v152, v152, v82, vcc
	v_cmp_eq_u32_e32 vcc, 3, v157
	v_lshrrev_b32_sdwa v160, v165, v159 dst_sel:DWORD dst_unused:UNUSED_PAD src0_sel:DWORD src1_sel:WORD_0
	v_lshrrev_b32_sdwa v161, v165, v159 dst_sel:DWORD dst_unused:UNUSED_PAD src0_sel:DWORD src1_sel:WORD_1
	v_cndmask_b32_e32 v163, v164, v15, vcc
	v_cndmask_b32_e32 v153, v153, v83, vcc
	ds_add_u32 v160, v162 offset:34416
	ds_add_u32 v161, v163 offset:34416
	v_pk_add_f32 v[80:81], v[78:79], v[152:153] neg_lo:[0,1] neg_hi:[0,1]
	s_nop 0
	v_pk_fma_f32 v[6:7], v[80:81], v[80:81], v[166:167]
	ds_read_b128 v[76:79], v135
	v_and_b32_e32 v154, 3, v13
	v_bfe_u32 v155, v13, 2, 2
	v_bfe_u32 v156, v13, 4, 2
	v_bfe_u32 v157, v13, 6, 2
	v_pk_fma_f32 v[80:81], v[58:59], v[20:21], v[16:17] op_sel_hi:[1,0,0]
	v_pk_fma_f32 v[80:81], v[124:125], v[36:37], v[80:81] op_sel_hi:[1,0,1]
	s_nop 0
	v_exp_f32_e32 v82, v80
	v_exp_f32_e32 v83, v81
	v_cmp_eq_u32_e32 vcc, 1, v154
	v_cvt_pknorm_u16_f32 v158, v82, v83
	v_and_b32_e32 v159, s16, v158
	v_cndmask_b32_e32 v162, v164, v15, vcc
	v_cndmask_b32_e32 v150, 0, v82, vcc
	v_cmp_eq_u32_e32 vcc, 1, v155
	v_lshrrev_b32_sdwa v160, v165, v159 dst_sel:DWORD dst_unused:UNUSED_PAD src0_sel:DWORD src1_sel:WORD_0
	v_lshrrev_b32_sdwa v161, v165, v159 dst_sel:DWORD dst_unused:UNUSED_PAD src0_sel:DWORD src1_sel:WORD_1
	v_cndmask_b32_e32 v163, v164, v15, vcc
	v_cndmask_b32_e32 v151, 0, v83, vcc
	ds_add_u32 v160, v162 offset:1648
	ds_add_u32 v161, v163 offset:1648
	v_pk_fma_f32 v[80:81], v[58:59], v[20:21], v[16:17] op_sel:[0,1,1]
	v_pk_fma_f32 v[80:81], v[124:125], v[36:37], v[80:81] op_sel:[0,1,0]
	s_nop 0
	v_exp_f32_e32 v82, v80
	v_exp_f32_e32 v83, v81
	v_cmp_eq_u32_e32 vcc, 2, v154
	v_cvt_pknorm_u16_f32 v158, v82, v83
	v_and_b32_e32 v159, s16, v158
	v_cndmask_b32_e32 v162, v164, v15, vcc
	v_cndmask_b32_e32 v150, v150, v82, vcc
	v_cmp_eq_u32_e32 vcc, 2, v155
	v_lshrrev_b32_sdwa v160, v165, v159 dst_sel:DWORD dst_unused:UNUSED_PAD src0_sel:DWORD src1_sel:WORD_0
	v_lshrrev_b32_sdwa v161, v165, v159 dst_sel:DWORD dst_unused:UNUSED_PAD src0_sel:DWORD src1_sel:WORD_1
	v_cndmask_b32_e32 v163, v164, v15, vcc
	v_cndmask_b32_e32 v151, v151, v83, vcc
	ds_add_u32 v160, v162 offset:18032
	ds_add_u32 v161, v163 offset:18032
	v_pk_fma_f32 v[80:81], v[58:59], v[8:9], v[12:13] op_sel_hi:[1,0,0]
	v_pk_fma_f32 v[80:81], v[124:125], v[24:25], v[80:81] op_sel_hi:[1,0,1]
	s_nop 0
	v_exp_f32_e32 v82, v80
	v_exp_f32_e32 v83, v81
	v_cmp_eq_u32_e32 vcc, 3, v154
	v_cvt_pknorm_u16_f32 v158, v82, v83
	v_and_b32_e32 v159, s16, v158
	v_cndmask_b32_e32 v162, v164, v15, vcc
	v_cndmask_b32_e32 v150, v150, v82, vcc
	v_cmp_eq_u32_e32 vcc, 3, v155
	v_lshrrev_b32_sdwa v160, v165, v159 dst_sel:DWORD dst_unused:UNUSED_PAD src0_sel:DWORD src1_sel:WORD_0
	v_lshrrev_b32_sdwa v161, v165, v159 dst_sel:DWORD dst_unused:UNUSED_PAD src0_sel:DWORD src1_sel:WORD_1
	v_cndmask_b32_e32 v163, v164, v15, vcc
	v_cndmask_b32_e32 v151, v151, v83, vcc
	ds_add_u32 v160, v162 offset:34416
	ds_add_u32 v161, v163 offset:34416
	s_waitcnt lgkmcnt(6)
	v_pk_add_f32 v[166:167], v[76:77], v[150:151] neg_lo:[0,1] neg_hi:[0,1]
	s_nop 0
	v_pk_fma_f32 v[166:167], v[166:167], v[166:167], v[6:7]
	v_pk_fma_f32 v[80:81], v[60:61], v[20:21], v[16:17] op_sel_hi:[1,0,0]
	v_pk_fma_f32 v[80:81], v[126:127], v[36:37], v[80:81] op_sel_hi:[1,0,1]
	s_nop 0
	v_exp_f32_e32 v82, v80
	v_exp_f32_e32 v83, v81
	v_cmp_eq_u32_e32 vcc, 1, v156
	v_cvt_pknorm_u16_f32 v158, v82, v83
	v_and_b32_e32 v159, s16, v158
	v_cndmask_b32_e32 v162, v164, v15, vcc
	v_cndmask_b32_e32 v152, 0, v82, vcc
	v_cmp_eq_u32_e32 vcc, 1, v157
	v_lshrrev_b32_sdwa v160, v165, v159 dst_sel:DWORD dst_unused:UNUSED_PAD src0_sel:DWORD src1_sel:WORD_0
	v_lshrrev_b32_sdwa v161, v165, v159 dst_sel:DWORD dst_unused:UNUSED_PAD src0_sel:DWORD src1_sel:WORD_1
	v_cndmask_b32_e32 v163, v164, v15, vcc
	v_cndmask_b32_e32 v153, 0, v83, vcc
	ds_add_u32 v160, v162 offset:1648
	ds_add_u32 v161, v163 offset:1648
	v_pk_fma_f32 v[80:81], v[60:61], v[20:21], v[16:17] op_sel:[0,1,1]
	v_pk_fma_f32 v[80:81], v[126:127], v[36:37], v[80:81] op_sel:[0,1,0]
	s_nop 0
	v_exp_f32_e32 v82, v80
	v_exp_f32_e32 v83, v81
	v_cmp_eq_u32_e32 vcc, 2, v156
	v_cvt_pknorm_u16_f32 v158, v82, v83
	v_and_b32_e32 v159, s16, v158
	v_cndmask_b32_e32 v162, v164, v15, vcc
	v_cndmask_b32_e32 v152, v152, v82, vcc
	v_cmp_eq_u32_e32 vcc, 2, v157
	v_lshrrev_b32_sdwa v160, v165, v159 dst_sel:DWORD dst_unused:UNUSED_PAD src0_sel:DWORD src1_sel:WORD_0
	v_lshrrev_b32_sdwa v161, v165, v159 dst_sel:DWORD dst_unused:UNUSED_PAD src0_sel:DWORD src1_sel:WORD_1
	v_cndmask_b32_e32 v163, v164, v15, vcc
	v_cndmask_b32_e32 v153, v153, v83, vcc
	ds_add_u32 v160, v162 offset:18032
	ds_add_u32 v161, v163 offset:18032
	v_pk_fma_f32 v[80:81], v[60:61], v[8:9], v[12:13] op_sel_hi:[1,0,0]
	v_pk_fma_f32 v[80:81], v[126:127], v[24:25], v[80:81] op_sel_hi:[1,0,1]
	s_nop 0
	v_exp_f32_e32 v82, v80
	v_exp_f32_e32 v83, v81
	v_cmp_eq_u32_e32 vcc, 3, v156
	v_cvt_pknorm_u16_f32 v158, v82, v83
	v_and_b32_e32 v159, s16, v158
	v_cndmask_b32_e32 v162, v164, v15, vcc
	v_cndmask_b32_e32 v152, v152, v82, vcc
	v_cmp_eq_u32_e32 vcc, 3, v157
	v_lshrrev_b32_sdwa v160, v165, v159 dst_sel:DWORD dst_unused:UNUSED_PAD src0_sel:DWORD src1_sel:WORD_0
	v_lshrrev_b32_sdwa v161, v165, v159 dst_sel:DWORD dst_unused:UNUSED_PAD src0_sel:DWORD src1_sel:WORD_1
	v_cndmask_b32_e32 v163, v164, v15, vcc
	v_cndmask_b32_e32 v153, v153, v83, vcc
	ds_add_u32 v160, v162 offset:34416
	ds_add_u32 v161, v163 offset:34416
	v_pk_add_f32 v[80:81], v[78:79], v[152:153] neg_lo:[0,1] neg_hi:[0,1]
	s_nop 0
	v_pk_fma_f32 v[6:7], v[80:81], v[80:81], v[166:167]
	ds_read_b128 v[76:79], v70
	v_and_b32_e32 v154, 3, v9
	v_bfe_u32 v155, v9, 2, 2
	v_bfe_u32 v156, v9, 4, 2
	v_bfe_u32 v157, v9, 6, 2
	v_pk_fma_f32 v[80:81], v[62:63], v[20:21], v[16:17] op_sel_hi:[1,0,0]
	v_pk_fma_f32 v[80:81], v[66:67], v[36:37], v[80:81] op_sel_hi:[1,0,1]
	s_nop 0
	v_exp_f32_e32 v82, v80
	v_exp_f32_e32 v83, v81
	v_cmp_eq_u32_e32 vcc, 1, v154
	v_cvt_pknorm_u16_f32 v158, v82, v83
	v_and_b32_e32 v159, s16, v158
	v_cndmask_b32_e32 v162, v164, v15, vcc
	v_cndmask_b32_e32 v150, 0, v82, vcc
	v_cmp_eq_u32_e32 vcc, 1, v155
	v_lshrrev_b32_sdwa v160, v165, v159 dst_sel:DWORD dst_unused:UNUSED_PAD src0_sel:DWORD src1_sel:WORD_0
	v_lshrrev_b32_sdwa v161, v165, v159 dst_sel:DWORD dst_unused:UNUSED_PAD src0_sel:DWORD src1_sel:WORD_1
	v_cndmask_b32_e32 v163, v164, v15, vcc
	v_cndmask_b32_e32 v151, 0, v83, vcc
	ds_add_u32 v160, v162 offset:1648
	ds_add_u32 v161, v163 offset:1648
	v_pk_fma_f32 v[80:81], v[62:63], v[20:21], v[16:17] op_sel:[0,1,1]
	v_pk_fma_f32 v[80:81], v[66:67], v[36:37], v[80:81] op_sel:[0,1,0]
	s_nop 0
	v_exp_f32_e32 v82, v80
	v_exp_f32_e32 v83, v81
	v_cmp_eq_u32_e32 vcc, 2, v154
	v_cvt_pknorm_u16_f32 v158, v82, v83
	v_and_b32_e32 v159, s16, v158
	v_cndmask_b32_e32 v162, v164, v15, vcc
	v_cndmask_b32_e32 v150, v150, v82, vcc
	v_cmp_eq_u32_e32 vcc, 2, v155
	v_lshrrev_b32_sdwa v160, v165, v159 dst_sel:DWORD dst_unused:UNUSED_PAD src0_sel:DWORD src1_sel:WORD_0
	v_lshrrev_b32_sdwa v161, v165, v159 dst_sel:DWORD dst_unused:UNUSED_PAD src0_sel:DWORD src1_sel:WORD_1
	v_cndmask_b32_e32 v163, v164, v15, vcc
	v_cndmask_b32_e32 v151, v151, v83, vcc
	ds_add_u32 v160, v162 offset:18032
	ds_add_u32 v161, v163 offset:18032
	v_pk_fma_f32 v[80:81], v[62:63], v[8:9], v[12:13] op_sel_hi:[1,0,0]
	v_pk_fma_f32 v[80:81], v[66:67], v[24:25], v[80:81] op_sel_hi:[1,0,1]
	s_nop 0
	v_exp_f32_e32 v82, v80
	v_exp_f32_e32 v83, v81
	v_cmp_eq_u32_e32 vcc, 3, v154
	v_cvt_pknorm_u16_f32 v158, v82, v83
	v_and_b32_e32 v159, s16, v158
	v_cndmask_b32_e32 v162, v164, v15, vcc
	v_cndmask_b32_e32 v150, v150, v82, vcc
	v_cmp_eq_u32_e32 vcc, 3, v155
	v_lshrrev_b32_sdwa v160, v165, v159 dst_sel:DWORD dst_unused:UNUSED_PAD src0_sel:DWORD src1_sel:WORD_0
	v_lshrrev_b32_sdwa v161, v165, v159 dst_sel:DWORD dst_unused:UNUSED_PAD src0_sel:DWORD src1_sel:WORD_1
	v_cndmask_b32_e32 v163, v164, v15, vcc
	v_cndmask_b32_e32 v151, v151, v83, vcc
	ds_add_u32 v160, v162 offset:34416
	ds_add_u32 v161, v163 offset:34416
	s_waitcnt lgkmcnt(6)
	v_pk_add_f32 v[166:167], v[76:77], v[150:151] neg_lo:[0,1] neg_hi:[0,1]
	s_nop 0
	v_pk_fma_f32 v[166:167], v[166:167], v[166:167], v[6:7]
	v_pk_fma_f32 v[80:81], v[64:65], v[20:21], v[16:17] op_sel_hi:[1,0,0]
	v_pk_fma_f32 v[80:81], v[68:69], v[36:37], v[80:81] op_sel_hi:[1,0,1]
	s_nop 0
	v_exp_f32_e32 v82, v80
	v_exp_f32_e32 v83, v81
	v_cmp_eq_u32_e32 vcc, 1, v156
	v_cvt_pknorm_u16_f32 v158, v82, v83
	v_and_b32_e32 v159, s16, v158
	v_cndmask_b32_e32 v162, v164, v15, vcc
	v_cndmask_b32_e32 v152, 0, v82, vcc
	v_cmp_eq_u32_e32 vcc, 1, v157
	v_lshrrev_b32_sdwa v160, v165, v159 dst_sel:DWORD dst_unused:UNUSED_PAD src0_sel:DWORD src1_sel:WORD_0
	v_lshrrev_b32_sdwa v161, v165, v159 dst_sel:DWORD dst_unused:UNUSED_PAD src0_sel:DWORD src1_sel:WORD_1
	v_cndmask_b32_e32 v163, v164, v15, vcc
	v_cndmask_b32_e32 v153, 0, v83, vcc
	ds_add_u32 v160, v162 offset:1648
	ds_add_u32 v161, v163 offset:1648
	v_pk_fma_f32 v[80:81], v[64:65], v[20:21], v[16:17] op_sel:[0,1,1]
	v_pk_fma_f32 v[80:81], v[68:69], v[36:37], v[80:81] op_sel:[0,1,0]
	s_nop 0
	v_exp_f32_e32 v82, v80
	v_exp_f32_e32 v83, v81
	v_cmp_eq_u32_e32 vcc, 2, v156
	v_cvt_pknorm_u16_f32 v158, v82, v83
	v_and_b32_e32 v159, s16, v158
	v_cndmask_b32_e32 v162, v164, v15, vcc
	v_cndmask_b32_e32 v152, v152, v82, vcc
	v_cmp_eq_u32_e32 vcc, 2, v157
	v_lshrrev_b32_sdwa v160, v165, v159 dst_sel:DWORD dst_unused:UNUSED_PAD src0_sel:DWORD src1_sel:WORD_0
	v_lshrrev_b32_sdwa v161, v165, v159 dst_sel:DWORD dst_unused:UNUSED_PAD src0_sel:DWORD src1_sel:WORD_1
	v_cndmask_b32_e32 v163, v164, v15, vcc
	v_cndmask_b32_e32 v153, v153, v83, vcc
	ds_add_u32 v160, v162 offset:18032
	ds_add_u32 v161, v163 offset:18032
	v_pk_fma_f32 v[80:81], v[64:65], v[8:9], v[12:13] op_sel_hi:[1,0,0]
	v_pk_fma_f32 v[80:81], v[68:69], v[24:25], v[80:81] op_sel_hi:[1,0,1]
	s_nop 0
	v_exp_f32_e32 v82, v80
	v_exp_f32_e32 v83, v81
	v_cmp_eq_u32_e32 vcc, 3, v156
	v_cvt_pknorm_u16_f32 v158, v82, v83
	v_and_b32_e32 v159, s16, v158
	v_cndmask_b32_e32 v162, v164, v15, vcc
	v_cndmask_b32_e32 v152, v152, v82, vcc
	v_cmp_eq_u32_e32 vcc, 3, v157
	v_lshrrev_b32_sdwa v160, v165, v159 dst_sel:DWORD dst_unused:UNUSED_PAD src0_sel:DWORD src1_sel:WORD_0
	v_lshrrev_b32_sdwa v161, v165, v159 dst_sel:DWORD dst_unused:UNUSED_PAD src0_sel:DWORD src1_sel:WORD_1
	v_cndmask_b32_e32 v163, v164, v15, vcc
	v_cndmask_b32_e32 v153, v153, v83, vcc
	ds_add_u32 v160, v162 offset:34416
	ds_add_u32 v161, v163 offset:34416
	v_pk_add_f32 v[80:81], v[78:79], v[152:153] neg_lo:[0,1] neg_hi:[0,1]
	s_nop 0
	v_pk_fma_f32 v[6:7], v[80:81], v[80:81], v[166:167]
	s_and_saveexec_b64 s[8:9], s[4:5]
	s_cbranch_execz .LBB0_60
	v_add_u32_e32 v149, 0x18000, v1
	ds_read_b128 v[76:79], v149
	v_and_b32_e32 v154, 3, v40
	v_bfe_u32 v155, v40, 2, 2
	v_bfe_u32 v156, v40, 4, 2
	v_bfe_u32 v157, v40, 6, 2
	v_pk_fma_f32 v[80:81], v[54:55], v[20:21], v[16:17] op_sel_hi:[1,0,0]
	v_pk_fma_f32 v[80:81], v[50:51], v[36:37], v[80:81] op_sel_hi:[1,0,1]
	s_nop 0
	v_exp_f32_e32 v82, v80
	v_exp_f32_e32 v83, v81
	v_cmp_eq_u32_e32 vcc, 1, v154
	v_cvt_pknorm_u16_f32 v158, v82, v83
	v_and_b32_e32 v159, s16, v158
	v_cndmask_b32_e32 v162, v164, v15, vcc
	v_cndmask_b32_e32 v150, 0, v82, vcc
	v_cmp_eq_u32_e32 vcc, 1, v155
	v_lshrrev_b32_sdwa v160, v165, v159 dst_sel:DWORD dst_unused:UNUSED_PAD src0_sel:DWORD src1_sel:WORD_0
	v_lshrrev_b32_sdwa v161, v165, v159 dst_sel:DWORD dst_unused:UNUSED_PAD src0_sel:DWORD src1_sel:WORD_1
	v_cndmask_b32_e32 v163, v164, v15, vcc
	v_cndmask_b32_e32 v151, 0, v83, vcc
	ds_add_u32 v160, v162 offset:1648
	ds_add_u32 v161, v163 offset:1648
	v_pk_fma_f32 v[80:81], v[54:55], v[20:21], v[16:17] op_sel:[0,1,1]
	v_pk_fma_f32 v[80:81], v[50:51], v[36:37], v[80:81] op_sel:[0,1,0]
	s_nop 0
	v_exp_f32_e32 v82, v80
	v_exp_f32_e32 v83, v81
	v_cmp_eq_u32_e32 vcc, 2, v154
	v_cvt_pknorm_u16_f32 v158, v82, v83
	v_and_b32_e32 v159, s16, v158
	v_cndmask_b32_e32 v162, v164, v15, vcc
	v_cndmask_b32_e32 v150, v150, v82, vcc
	v_cmp_eq_u32_e32 vcc, 2, v155
	v_lshrrev_b32_sdwa v160, v165, v159 dst_sel:DWORD dst_unused:UNUSED_PAD src0_sel:DWORD src1_sel:WORD_0
	v_lshrrev_b32_sdwa v161, v165, v159 dst_sel:DWORD dst_unused:UNUSED_PAD src0_sel:DWORD src1_sel:WORD_1
	v_cndmask_b32_e32 v163, v164, v15, vcc
	v_cndmask_b32_e32 v151, v151, v83, vcc
	ds_add_u32 v160, v162 offset:18032
	ds_add_u32 v161, v163 offset:18032
	v_pk_fma_f32 v[80:81], v[54:55], v[8:9], v[12:13] op_sel_hi:[1,0,0]
	v_pk_fma_f32 v[80:81], v[50:51], v[24:25], v[80:81] op_sel_hi:[1,0,1]
	s_nop 0
	v_exp_f32_e32 v82, v80
	v_exp_f32_e32 v83, v81
	v_cmp_eq_u32_e32 vcc, 3, v154
	v_cvt_pknorm_u16_f32 v158, v82, v83
	v_and_b32_e32 v159, s16, v158
	v_cndmask_b32_e32 v162, v164, v15, vcc
	v_cndmask_b32_e32 v150, v150, v82, vcc
	v_cmp_eq_u32_e32 vcc, 3, v155
	v_lshrrev_b32_sdwa v160, v165, v159 dst_sel:DWORD dst_unused:UNUSED_PAD src0_sel:DWORD src1_sel:WORD_0
	v_lshrrev_b32_sdwa v161, v165, v159 dst_sel:DWORD dst_unused:UNUSED_PAD src0_sel:DWORD src1_sel:WORD_1
	v_cndmask_b32_e32 v163, v164, v15, vcc
	v_cndmask_b32_e32 v151, v151, v83, vcc
	ds_add_u32 v160, v162 offset:34416
	ds_add_u32 v161, v163 offset:34416
	s_waitcnt lgkmcnt(6)
	v_pk_add_f32 v[166:167], v[76:77], v[150:151] neg_lo:[0,1] neg_hi:[0,1]
	s_nop 0
	v_pk_fma_f32 v[166:167], v[166:167], v[166:167], v[6:7]
	v_pk_fma_f32 v[80:81], v[46:47], v[20:21], v[16:17] op_sel_hi:[1,0,0]
	v_pk_fma_f32 v[80:81], v[74:75], v[36:37], v[80:81] op_sel_hi:[1,0,1]
	s_nop 0
	v_exp_f32_e32 v82, v80
	v_exp_f32_e32 v83, v81
	v_cmp_eq_u32_e32 vcc, 1, v156
	v_cvt_pknorm_u16_f32 v158, v82, v83
	v_and_b32_e32 v159, s16, v158
	v_cndmask_b32_e32 v162, v164, v15, vcc
	v_cndmask_b32_e32 v152, 0, v82, vcc
	v_cmp_eq_u32_e32 vcc, 1, v157
	v_lshrrev_b32_sdwa v160, v165, v159 dst_sel:DWORD dst_unused:UNUSED_PAD src0_sel:DWORD src1_sel:WORD_0
	v_lshrrev_b32_sdwa v161, v165, v159 dst_sel:DWORD dst_unused:UNUSED_PAD src0_sel:DWORD src1_sel:WORD_1
	v_cndmask_b32_e32 v163, v164, v15, vcc
	v_cndmask_b32_e32 v153, 0, v83, vcc
	ds_add_u32 v160, v162 offset:1648
	ds_add_u32 v161, v163 offset:1648
	v_pk_fma_f32 v[80:81], v[46:47], v[20:21], v[16:17] op_sel:[0,1,1]
	v_pk_fma_f32 v[80:81], v[74:75], v[36:37], v[80:81] op_sel:[0,1,0]
	s_nop 0
	v_exp_f32_e32 v82, v80
	v_exp_f32_e32 v83, v81
	v_cmp_eq_u32_e32 vcc, 2, v156
	v_cvt_pknorm_u16_f32 v158, v82, v83
	v_and_b32_e32 v159, s16, v158
	v_cndmask_b32_e32 v162, v164, v15, vcc
	v_cndmask_b32_e32 v152, v152, v82, vcc
	v_cmp_eq_u32_e32 vcc, 2, v157
	v_lshrrev_b32_sdwa v160, v165, v159 dst_sel:DWORD dst_unused:UNUSED_PAD src0_sel:DWORD src1_sel:WORD_0
	v_lshrrev_b32_sdwa v161, v165, v159 dst_sel:DWORD dst_unused:UNUSED_PAD src0_sel:DWORD src1_sel:WORD_1
	v_cndmask_b32_e32 v163, v164, v15, vcc
	v_cndmask_b32_e32 v153, v153, v83, vcc
	ds_add_u32 v160, v162 offset:18032
	ds_add_u32 v161, v163 offset:18032
	v_pk_fma_f32 v[80:81], v[46:47], v[8:9], v[12:13] op_sel_hi:[1,0,0]
	v_pk_fma_f32 v[80:81], v[74:75], v[24:25], v[80:81] op_sel_hi:[1,0,1]
	s_nop 0
	v_exp_f32_e32 v82, v80
	v_exp_f32_e32 v83, v81
	v_cmp_eq_u32_e32 vcc, 3, v156
	v_cvt_pknorm_u16_f32 v158, v82, v83
	v_and_b32_e32 v159, s16, v158
	v_cndmask_b32_e32 v162, v164, v15, vcc
	v_cndmask_b32_e32 v152, v152, v82, vcc
	v_cmp_eq_u32_e32 vcc, 3, v157
	v_lshrrev_b32_sdwa v160, v165, v159 dst_sel:DWORD dst_unused:UNUSED_PAD src0_sel:DWORD src1_sel:WORD_0
	v_lshrrev_b32_sdwa v161, v165, v159 dst_sel:DWORD dst_unused:UNUSED_PAD src0_sel:DWORD src1_sel:WORD_1
	v_cndmask_b32_e32 v163, v164, v15, vcc
	v_cndmask_b32_e32 v153, v153, v83, vcc
	ds_add_u32 v160, v162 offset:34416
	ds_add_u32 v161, v163 offset:34416
	v_pk_add_f32 v[80:81], v[78:79], v[152:153] neg_lo:[0,1] neg_hi:[0,1]
	s_nop 0
	v_pk_fma_f32 v[6:7], v[80:81], v[80:81], v[166:167]
